# f8 + second half: first K reads right after the barrier, LDS-DMA pieces spread across the first QK MFMA gaps
# speedup vs baseline: 1.0062x; 1.0021x over previous
; #define LAS __attribute__((address_space(3)))
; #define VM0() asm volatile("s_waitcnt vmcnt(0)" ::: "memory")
; #define B_RESC(a, rare) do { if (rare) { if (hi == 0) al_l[r32] = (a); asm volatile("s_waitcnt lgkmcnt(0)" ::: "memory"); __builtin_amdgcn_wave_barrier(); \
;         _Pragma("unroll") for (int _d = 0; _d < 2; ++_d) _Pragma("unroll") for (int _r = 0; _r < 16; ++_r) o[_d][_r] *= al_l[crow(_r, hi)]; C_SPLAT(); } } while (0)
; #define C_SPLAT() do { _Pragma("unroll") for (int _r = 0; _r < 16; ++_r) cinit[_r] = -m_reg; asm volatile("" : "+v"(cinit)); } while (0)
; DEVI void attn_unit8(const Params& p, char* smem, int unit, int l, int& cvs  , CvRun& crun) {
;     ...
;     LAS char* const Kl = (LAS char*)K_lds + wid * 1024; LAS char* const Vl = (LAS char*)V_lds + wid * 1024;
;     ...
;     B_DMA(0, 0); B_DMA(1, 1); VM0(); __syncthreads();
;     f32x16 cinit;
;     ...
;     { f32x16 z; _Pragma("unroll") for (int r = 0; r < 16; ++r) z[r] = 0.f;
;       qkt(pA0, pA1, K_lds, qr, r32, hi, z); } partialSM<true>(pA0, pA1, m_reg, alA); C_SPLAT();
;     int s0 = 0, s1 = 1, s2 = 2;
;     for (int T = 0; T + 1 < NTILE; ++T) {
;         const char* Kb = K_lds + s0 * 24576; const int vb = vb0 + s0 * 16384;
;         CvRegs cvr; cv_issue(p, l, cvs, lane, cvr, crun); cvs += (int)gridDim.x * 8;
;         qkt(pB0, pB1, Kb + 12288, qr, r32, hi, cinit);
;         finishSM(pA0, pA1, alA, l_reg, pa0, pa1, pa2, pa3);
;         pv_both(o[0], o[1], vb, pa0, pa1, pa2, pa3);
;         { const bool rr_ = partialSM<false>(pB0, pB1, m_reg, alB); B_RESC(alB, rr_); }
;         cv_finish(smem + 124928 + wid * 2304, lane, cvr);
;         if (cvr.live) asm volatile("s_waitcnt vmcnt(2)" ::: "memory"); else VM0();
;         __syncthreads();
;         if (T + 2 < NTILE) B_DMA(T + 2, s2);
;         qkt(pA0, pA1, K_lds + s1 * 24576, qr, r32, hi, cinit);
;         finishSM(pB0, pB1, alB, l_reg, pa0, pa1, pa2, pa3);
;         pv_both(o[0], o[1], vb + 8192, pa0, pa1, pa2, pa3);
;         { const bool rr_ = partialSM<false>(pA0, pA1, m_reg, alA); B_RESC(alA, rr_); }
.LBB0_702:
	s_mul_i32 s98, s2, 0x6000
	s_add_i32 s98, s96, s98
	s_lshl_b32 s99, s2, 14
	s_add_i32 s99, s97, s99
	s_mul_i32 s6, s61, 0x6000
	s_add_i32 s6, s6, 0
	v_add_u32_e32 v86, s6, v129
	v_lshl_add_u64 v[250:251], v[118:119], 0, s[12:13]
	s_mov_b32 m0, s98
	s_barrier
	ds_read_b128 v[82:85], v86
	ds_read_b128 v[210:213], v86 offset:6144
	global_load_lds_dwordx4 v[250:251], off
	v_exp_f32_e32 v66, v66
	s_waitcnt lgkmcnt(1)
	v_mfma_f32_32x32x16_bf16 v[98:113], v[82:85], v[150:153], v[34:49]
	v_add_u32_e32 v126, s6, v184
	v_lshl_add_u64 v[250:251], v[120:121], 0, s[12:13]
	s_add_i32 m0, s98, 0x2000
	v_exp_f32_e32 v67, v67
	v_exp_f32_e32 v68, v68
	global_load_lds_dwordx4 v[250:251], off
	v_exp_f32_e32 v69, v69
	v_exp_f32_e32 v70, v70
	v_exp_f32_e32 v71, v71
	v_exp_f32_e32 v72, v72
	s_waitcnt lgkmcnt(0)
	v_mfma_f32_32x32x16_bf16 v[82:97], v[210:213], v[150:153], v[34:49]
	ds_read_b128 v[210:213], v126
	ds_read_b128 v[214:217], v126 offset:6144
	v_add_u32_e32 v126, s6, v185
	v_lshl_add_u64 v[250:251], v[122:123], 0, s[12:13]
	s_add_i32 m0, s98, 0x4000
	v_exp_f32_e32 v73, v73
	v_exp_f32_e32 v74, v74
	global_load_lds_dwordx4 v[250:251], off
	v_exp_f32_e32 v75, v75
	v_exp_f32_e32 v76, v76
	v_exp_f32_e32 v77, v77
	s_waitcnt lgkmcnt(1)
	v_mfma_f32_32x32x16_bf16 v[98:113], v[210:213], v[138:141], v[98:113]
	s_mov_b32 m0, s99
	v_exp_f32_e32 v78, v78
	v_exp_f32_e32 v79, v79
	v_lshl_add_u64 v[250:251], v[116:117], 0, s[40:41]
	global_load_lds_dwordx4 v[116:117], off
	s_add_i32 m0, s99, 0x2000
	v_exp_f32_e32 v80, v80
	v_exp_f32_e32 v81, v81
	v_add_u32_e32 v174, 0x2000, v202
	global_load_lds_dwordx4 v[250:251], off
	s_waitcnt lgkmcnt(0)
	v_mfma_f32_32x32x16_bf16 v[82:97], v[214:217], v[138:141], v[82:97]
	ds_read_b128 v[210:213], v126
	ds_read_b128 v[214:217], v126 offset:6144
	v_add_u32_e32 v126, s6, v204
	s_waitcnt lgkmcnt(1)
	v_mfma_f32_32x32x16_bf16 v[98:113], v[210:213], v[134:137], v[98:113]
	ds_read_b128 v[210:213], v126
	ds_read_b128 v[218:221], v126 offset:6144
	v_add_u32_e32 v126, s6, v205
	s_waitcnt lgkmcnt(2)
	v_mfma_f32_32x32x16_bf16 v[82:97], v[214:217], v[134:137], v[82:97]
	ds_read_b128 v[214:217], v126
	ds_read_b128 v[222:225], v126 offset:6144
	v_add_u32_e32 v126, s6, v206
	ds_read_b128 v[226:229], v126
	ds_read_b128 v[230:233], v126 offset:6144
	v_pk_add_f32 v[126:127], v[50:51], v[66:67]
	v_cvt_pk_bf16_f32 v50, v50, v51
	v_cvt_pk_bf16_f32 v51, v52, v53
	s_waitcnt lgkmcnt(5)
	v_mfma_f32_32x32x16_bf16 v[98:113], v[210:213], v[130:133], v[98:113]
	v_add_f32_e64 v210, v52, v68
	v_add_f32_e64 v211, v53, v69
	v_cvt_pk_bf16_f32 v52, v54, v55
	v_cvt_pk_bf16_f32 v53, v56, v57
	v_add_f32_e64 v126, v210, v126
	v_add_f32_e64 v127, v211, v127
	v_add_f32_e64 v210, v54, v70
	v_add_f32_e64 v211, v55, v71
	v_cvt_pk_bf16_f32 v54, v58, v59
	s_waitcnt lgkmcnt(4)
	v_mfma_f32_32x32x16_bf16 v[82:97], v[218:221], v[130:133], v[82:97]
	v_add_f32_e64 v126, v210, v126
	v_add_f32_e64 v127, v211, v127
	v_add_f32_e64 v210, v56, v72
	v_add_f32_e64 v211, v57, v73
	v_cvt_pk_bf16_f32 v55, v60, v61
	v_cvt_pk_bf16_f32 v56, v62, v63
	v_cvt_pk_bf16_f32 v57, v64, v65
	v_add_f32_e64 v126, v210, v126
	v_add_f32_e64 v127, v211, v127
	v_pk_add_f32 v[210:211], v[58:59], v[74:75]
	v_cvt_pk_bf16_f32 v58, v66, v67
	v_cvt_pk_bf16_f32 v59, v68, v69
	s_waitcnt lgkmcnt(3)
	v_mfma_f32_32x32x16_bf16 v[98:113], v[214:217], v[146:149], v[98:113]
	v_add_f32_e64 v126, v210, v126
	v_add_f32_e64 v127, v211, v127
	v_add_f32_e64 v210, v60, v76
	v_add_f32_e64 v211, v61, v77
	v_cvt_pk_bf16_f32 v60, v70, v71
	v_cvt_pk_bf16_f32 v61, v72, v73
	v_add_f32_e64 v126, v210, v126
	v_add_f32_e64 v127, v211, v127
	v_pk_add_f32 v[210:211], v[62:63], v[78:79]
	v_cvt_pk_bf16_f32 v62, v74, v75
	v_cvt_pk_bf16_f32 v63, v76, v77
	s_waitcnt lgkmcnt(2)
; template <bool FIRST> DEVI bool partialSM(f32x16& p0, f32x16& p1, float& m_reg, float& alpha) {
;     float pmax = p0[0];
; #pragma unroll
;     for (int r = 1; r < 16; ++r) pmax = fmaxf(pmax, p0[r]);
; #pragma unroll
;     for (int r = 0; r < 16; ++r) pmax = fmaxf(pmax, p1[r]);
;     { auto rr = __builtin_amdgcn_permlane32_swap(__float_as_uint(pmax), __float_as_uint(pmax), false, false);
;       pmax = fmaxf(__uint_as_float(rr[0]), __uint_as_float(rr[1])); }
;     if (FIRST) { m_reg = pmax; alpha = 1.f;
; #pragma unroll
;         for (int r = 0; r < 16; ++r) { p0[r] = __builtin_amdgcn_exp2f(p0[r] - pmax); p1[r] = p1[r] - pmax; }
;         return false;
;     } else if (__builtin_expect(__all(pmax <= ATT_THR), 1)) { alpha = 1.f;
; #pragma unroll
;         for (int r = 0; r < 16; ++r) p0[r] = __builtin_amdgcn_exp2f(p0[r]);
;         return false;
;     } else { const float d = fmaxf(pmax, 0.f); alpha = __builtin_amdgcn_exp2f(-d); m_reg += d;
; #pragma unroll
;         for (int r = 0; r < 16; ++r) { p0[r] = __builtin_amdgcn_exp2f(p0[r] - d); p1[r] = p1[r] - d; }
;         return true;
;     }
; }
; DEVI void finishSM(f32x16& p0, f32x16& p1, float alpha, float& l_reg, bf16x8& pa0, bf16x8& pa1, bf16x8& pa2, bf16x8& pa3) {
; #pragma unroll
;     for (int r = 0; r < 16; ++r) p1[r] = __builtin_amdgcn_exp2f(p1[r]);
;     f32x2 s2 = (f32x2){p0[0], p0[1]} + (f32x2){p1[0], p1[1]};
; #pragma unroll
;     for (int r = 2; r < 16; r += 2) s2 += (f32x2){p0[r], p0[r + 1]} + (f32x2){p1[r], p1[r + 1]};
;     float ps = s2[0] + s2[1];
;     { auto rr = __builtin_amdgcn_permlane32_swap(__float_as_uint(ps), __float_as_uint(ps), false, false);
;       ps = __uint_as_float(rr[0]) + __uint_as_float(rr[1]); }
;     l_reg = l_reg * alpha + ps;
;     ...
;     PK4(p0, 0, pa0); PK4(p0, 8, pa1); PK4(p1, 0, pa2); PK4(p1, 8, pa3);
;     ...
; }
; DEVI void qkt(f32x16& p0, f32x16& p1, const char* Kb, const bf16x8 (&qr)[6], int r32, int hi, const f32x16& cinit) {
; #pragma unroll
;     for (int d0 = 0; d0 < 6; ++d0) { const int cb = (d0 * 16 + hi * 8) * 2;
;         const bf16x8 k0 = *(const bf16x8*)(Kb + KSWZ(r32, cb)), k1 = *(const bf16x8*)(Kb + KSWZ(32 + r32, cb));
;         p0 = __builtin_amdgcn_mfma_f32_32x32x16_bf16(k0, qr[d0], d0 == 0 ? cinit : p0, 0, 0, 0);
;         p1 = __builtin_amdgcn_mfma_f32_32x32x16_bf16(k1, qr[d0], d0 == 0 ? cinit : p1, 0, 0, 0); }
; }
	v_mfma_f32_32x32x16_bf16 v[82:97], v[222:225], v[146:149], v[82:97]
	v_add_f32_e64 v126, v210, v126
	v_add_f32_e64 v127, v211, v127
	v_add_f32_e64 v210, v64, v80
	v_add_f32_e64 v211, v65, v81
	v_cvt_pk_bf16_f32 v64, v78, v79
	v_cvt_pk_bf16_f32 v65, v80, v81
	ds_read_b64_tr_b16 v[66:67], v174 offset:0
	ds_read_b64_tr_b16 v[68:69], v174 offset:0x400
	ds_read_b64_tr_b16 v[70:71], v174 offset:0x800
	ds_read_b64_tr_b16 v[72:73], v174 offset:0xc00
	ds_read_b64_tr_b16 v[74:75], v174 offset:0x1000
	ds_read_b64_tr_b16 v[76:77], v174 offset:0x1400
	ds_read_b64_tr_b16 v[78:79], v174 offset:0x1800
	ds_read_b64_tr_b16 v[80:81], v174 offset:0x1c00
	v_add_f32_e64 v126, v210, v126
	v_add_f32_e64 v127, v211, v127
	ds_read_b64_tr_b16 v[210:211], v174 offset:0x200
	ds_read_b64_tr_b16 v[212:213], v174 offset:0x600
	ds_read_b64_tr_b16 v[214:215], v174 offset:0xa00
	s_waitcnt lgkmcnt(12)
	v_mfma_f32_32x32x16_bf16 v[98:113], v[226:229], v[142:145], v[98:113]
	ds_read_b64_tr_b16 v[216:217], v174 offset:0xe00
	ds_read_b64_tr_b16 v[218:219], v174 offset:0x1200
	ds_read_b64_tr_b16 v[220:221], v174 offset:0x1600
	ds_read_b64_tr_b16 v[222:223], v174 offset:0x1a00
	ds_read_b64_tr_b16 v[224:225], v174 offset:0x1e00
	v_pk_add_f32 v[126:127], v[126:127], v[126:127] op_sel:[0,1] op_sel_hi:[1,0]
	s_waitcnt lgkmcnt(15)
	v_mfma_f32_32x32x16_bf16 v[82:97], v[230:233], v[142:145], v[82:97]
	v_mov_b32_e32 v127, v126
	s_nop 1
	v_permlane32_swap_b32_e32 v126, v127
	s_waitcnt lgkmcnt(14)
	v_mfma_f32_32x32x16_bf16 v[18:33], v[50:53], v[66:69], v[18:33]
	s_waitcnt lgkmcnt(12)
	v_mfma_f32_32x32x16_bf16 v[18:33], v[54:57], v[70:73], v[18:33]
	s_waitcnt lgkmcnt(10)
	v_mfma_f32_32x32x16_bf16 v[18:33], v[58:61], v[74:77], v[18:33]
	s_waitcnt lgkmcnt(8)
	v_mfma_f32_32x32x16_bf16 v[18:33], v[62:65], v[78:81], v[18:33]
	s_waitcnt lgkmcnt(6)
	v_mfma_f32_32x32x16_bf16 v[2:17], v[50:53], v[210:213], v[2:17]
	s_nop 0
	v_max_f32_e32 v249, v99, v99
	v_max_f32_e32 v250, v98, v98
	v_max_f32_e32 v249, v250, v249
	v_max3_f32 v249, v249, v100, v101
	v_max3_f32 v249, v249, v102, v103
	v_max3_f32 v251, v249, v104, v105
	v_max3_f32 v251, v251, v106, v107
	s_waitcnt lgkmcnt(4)
	v_exp_f32_e32 v50, v98
	v_exp_f32_e32 v51, v99
	v_exp_f32_e32 v52, v100
	v_exp_f32_e32 v53, v101
	v_mov_b64_e32 v[66:67], v[82:83]
	v_mov_b64_e32 v[68:69], v[84:85]
	v_mfma_f32_32x32x16_bf16 v[2:17], v[54:57], v[214:217], v[2:17]
	v_max3_f32 v251, v251, v108, v109
	v_max3_f32 v251, v251, v110, v111
	v_max3_f32 v251, v251, v112, v113
	v_max3_f32 v251, v251, v82, v83
	v_max3_f32 v251, v251, v84, v85
	v_max3_f32 v251, v251, v86, v87
	v_max3_f32 v251, v251, v88, v89
	s_waitcnt lgkmcnt(2)
	v_exp_f32_e32 v54, v102
	v_exp_f32_e32 v55, v103
	v_exp_f32_e32 v56, v104
	v_exp_f32_e32 v57, v105
	v_mov_b64_e32 v[70:71], v[86:87]
	v_mov_b64_e32 v[72:73], v[88:89]
	v_mfma_f32_32x32x16_bf16 v[2:17], v[58:61], v[218:221], v[2:17]
	v_max3_f32 v251, v251, v90, v91
	v_max3_f32 v251, v251, v92, v93
	v_max3_f32 v251, v251, v94, v95
	v_max3_f32 v251, v251, v96, v97
	v_mov_b32_e32 v252, v251
	s_nop 1
	v_permlane32_swap_b32_e32 v251, v252
	s_waitcnt lgkmcnt(0)
	v_exp_f32_e32 v58, v106
	v_exp_f32_e32 v59, v107
	v_exp_f32_e32 v60, v108
	v_exp_f32_e32 v61, v109
	v_mov_b64_e32 v[74:75], v[90:91]
	v_mov_b64_e32 v[76:77], v[92:93]
	v_mfma_f32_32x32x16_bf16 v[2:17], v[62:65], v[222:225], v[2:17]
	v_exp_f32_e32 v62, v110
	v_exp_f32_e32 v63, v111
	v_exp_f32_e32 v64, v112
	v_exp_f32_e32 v65, v113
	v_mov_b64_e32 v[78:79], v[94:95]
	v_mov_b64_e32 v[80:81], v[96:97]
	v_max_f32_e32 v252, v252, v252
	v_max_f32_e32 v251, v251, v251
	v_max_f32_e32 v174, v251, v252
	v_cmp_ge_f32_e32 vcc, s79, v174
	s_cmp_lg_u64 vcc, exec
	s_cselect_b64 s[6:7], -1, 0
	s_cbranch_scc1 .LBB0_711
	v_mov_b32_e32 v202, 1.0
	v_mov_b32_e32 v203, v209
	s_branch .LBB0_716

; #define LAS __attribute__((address_space(3)))
; #define VM0() asm volatile("s_waitcnt vmcnt(0)" ::: "memory")
; #define B_RESC(a, rare) do { if (rare) { if (hi == 0) al_l[r32] = (a); asm volatile("s_waitcnt lgkmcnt(0)" ::: "memory"); __builtin_amdgcn_wave_barrier(); \
;         _Pragma("unroll") for (int _d = 0; _d < 2; ++_d) _Pragma("unroll") for (int _r = 0; _r < 16; ++_r) o[_d][_r] *= al_l[crow(_r, hi)]; C_SPLAT(); } } while (0)
; #define C_SPLAT() do { _Pragma("unroll") for (int _r = 0; _r < 16; ++_r) cinit[_r] = -m_reg; asm volatile("" : "+v"(cinit)); } while (0)
; DEVI void attn_unit8(const Params& p, char* smem, int unit, int l, int& cvs  , CvRun& crun) {
;     ...
;     LAS char* const Kl = (LAS char*)K_lds + wid * 1024; LAS char* const Vl = (LAS char*)V_lds + wid * 1024;
;     ...
;     B_DMA(0, 0); B_DMA(1, 1); VM0(); __syncthreads();
;     f32x16 cinit;
;     ...
;     { f32x16 z; _Pragma("unroll") for (int r = 0; r < 16; ++r) z[r] = 0.f;
;       qkt(pA0, pA1, K_lds, qr, r32, hi, z); } partialSM<true>(pA0, pA1, m_reg, alA); C_SPLAT();
;     int s0 = 0, s1 = 1, s2 = 2;
;     for (int T = 0; T + 1 < NTILE; ++T) {
;         const char* Kb = K_lds + s0 * 24576; const int vb = vb0 + s0 * 16384;
;         CvRegs cvr; cv_issue(p, l, cvs, lane, cvr, crun); cvs += (int)gridDim.x * 8;
;         qkt(pB0, pB1, Kb + 12288, qr, r32, hi, cinit);
;         finishSM(pA0, pA1, alA, l_reg, pa0, pa1, pa2, pa3);
;         pv_both(o[0], o[1], vb, pa0, pa1, pa2, pa3);
;         { const bool rr_ = partialSM<false>(pB0, pB1, m_reg, alB); B_RESC(alB, rr_); }
;         cv_finish(smem + 124928 + wid * 2304, lane, cvr);
;         if (cvr.live) asm volatile("s_waitcnt vmcnt(2)" ::: "memory"); else VM0();
;         __syncthreads();
;         if (T + 2 < NTILE) B_DMA(T + 2, s2);
;         qkt(pA0, pA1, K_lds + s1 * 24576, qr, r32, hi, cinit);
;         finishSM(pB0, pB1, alB, l_reg, pa0, pa1, pa2, pa3);
;         pv_both(o[0], o[1], vb + 8192, pa0, pa1, pa2, pa3);
;         { const bool rr_ = partialSM<false>(pA0, pA1, m_reg, alA); B_RESC(alA, rr_); }
.LBB0_2266:
	s_mul_i32 s98, s61, 0x6000
	s_add_i32 s98, s96, s98
	s_lshl_b32 s99, s61, 14
	s_add_i32 s99, s97, s99
	s_mul_i32 s6, s2, 0x6000
	s_add_i32 s6, s6, 0
	v_add_u32_e32 v86, s6, v129
	v_lshl_add_u64 v[250:251], v[118:119], 0, s[12:13]
	s_mov_b32 m0, s98
	s_barrier
	ds_read_b128 v[82:85], v86
	ds_read_b128 v[212:215], v86 offset:6144
	global_load_lds_dwordx4 v[250:251], off
	v_exp_f32_e32 v66, v66
	s_waitcnt lgkmcnt(1)
	v_mfma_f32_32x32x16_bf16 v[98:113], v[82:85], v[150:153], v[34:49]
	v_add_u32_e32 v126, s6, v184
	v_lshl_add_u64 v[250:251], v[120:121], 0, s[12:13]
	s_add_i32 m0, s98, 0x2000
	v_exp_f32_e32 v67, v67
	v_exp_f32_e32 v68, v68
	global_load_lds_dwordx4 v[250:251], off
	v_exp_f32_e32 v69, v69
	v_exp_f32_e32 v70, v70
	v_exp_f32_e32 v71, v71
	v_exp_f32_e32 v72, v72
	s_waitcnt lgkmcnt(0)
	v_mfma_f32_32x32x16_bf16 v[82:97], v[212:215], v[150:153], v[34:49]
	ds_read_b128 v[212:215], v126
	ds_read_b128 v[216:219], v126 offset:6144
	v_add_u32_e32 v126, s6, v185
	v_lshl_add_u64 v[250:251], v[122:123], 0, s[12:13]
	s_add_i32 m0, s98, 0x4000
	v_exp_f32_e32 v73, v73
	v_exp_f32_e32 v74, v74
	global_load_lds_dwordx4 v[250:251], off
	v_exp_f32_e32 v75, v75
	v_exp_f32_e32 v76, v76
	v_exp_f32_e32 v77, v77
	s_waitcnt lgkmcnt(1)
	v_mfma_f32_32x32x16_bf16 v[98:113], v[212:215], v[138:141], v[98:113]
	s_mov_b32 m0, s99
	v_exp_f32_e32 v78, v78
	v_exp_f32_e32 v79, v79
	v_lshl_add_u64 v[250:251], v[116:117], 0, s[40:41]
	global_load_lds_dwordx4 v[116:117], off
	s_add_i32 m0, s99, 0x2000
	v_exp_f32_e32 v80, v80
	v_exp_f32_e32 v81, v81
	v_add_u32_e32 v174, 0x2000, v203
	global_load_lds_dwordx4 v[250:251], off
	s_waitcnt lgkmcnt(0)
	v_mfma_f32_32x32x16_bf16 v[82:97], v[216:219], v[138:141], v[82:97]
	ds_read_b128 v[212:215], v126
	ds_read_b128 v[216:219], v126 offset:6144
	v_add_u32_e32 v126, s6, v205
	s_waitcnt lgkmcnt(1)
	v_mfma_f32_32x32x16_bf16 v[98:113], v[212:215], v[134:137], v[98:113]
	ds_read_b128 v[212:215], v126
	ds_read_b128 v[220:223], v126 offset:6144
	v_add_u32_e32 v126, s6, v206
	s_waitcnt lgkmcnt(2)
	v_mfma_f32_32x32x16_bf16 v[82:97], v[216:219], v[134:137], v[82:97]
	ds_read_b128 v[216:219], v126
	ds_read_b128 v[224:227], v126 offset:6144
	v_add_u32_e32 v126, s6, v207
	ds_read_b128 v[228:231], v126
	ds_read_b128 v[232:235], v126 offset:6144
	v_pk_add_f32 v[126:127], v[50:51], v[66:67]
	v_cvt_pk_bf16_f32 v50, v50, v51
	v_cvt_pk_bf16_f32 v51, v52, v53
	s_waitcnt lgkmcnt(5)
	v_mfma_f32_32x32x16_bf16 v[98:113], v[212:215], v[130:133], v[98:113]
	v_add_f32_e64 v212, v52, v68
	v_add_f32_e64 v213, v53, v69
	v_cvt_pk_bf16_f32 v52, v54, v55
	v_cvt_pk_bf16_f32 v53, v56, v57
	v_add_f32_e64 v126, v212, v126
	v_add_f32_e64 v127, v213, v127
	v_add_f32_e64 v212, v54, v70
	v_add_f32_e64 v213, v55, v71
	v_cvt_pk_bf16_f32 v54, v58, v59
	s_waitcnt lgkmcnt(4)
	v_mfma_f32_32x32x16_bf16 v[82:97], v[220:223], v[130:133], v[82:97]
	v_add_f32_e64 v126, v212, v126
	v_add_f32_e64 v127, v213, v127
	v_add_f32_e64 v212, v56, v72
	v_add_f32_e64 v213, v57, v73
	v_cvt_pk_bf16_f32 v55, v60, v61
	v_cvt_pk_bf16_f32 v56, v62, v63
	v_cvt_pk_bf16_f32 v57, v64, v65
	v_add_f32_e64 v126, v212, v126
	v_add_f32_e64 v127, v213, v127
	v_pk_add_f32 v[212:213], v[58:59], v[74:75]
	v_cvt_pk_bf16_f32 v58, v66, v67
	v_cvt_pk_bf16_f32 v59, v68, v69
	s_waitcnt lgkmcnt(3)
	v_mfma_f32_32x32x16_bf16 v[98:113], v[216:219], v[146:149], v[98:113]
	v_add_f32_e64 v126, v212, v126
	v_add_f32_e64 v127, v213, v127
	v_add_f32_e64 v212, v60, v76
	v_add_f32_e64 v213, v61, v77
	v_cvt_pk_bf16_f32 v60, v70, v71
	v_cvt_pk_bf16_f32 v61, v72, v73
	v_add_f32_e64 v126, v212, v126
	v_add_f32_e64 v127, v213, v127
	v_pk_add_f32 v[212:213], v[62:63], v[78:79]
	v_cvt_pk_bf16_f32 v62, v74, v75
	v_cvt_pk_bf16_f32 v63, v76, v77
	s_waitcnt lgkmcnt(2)
; template <bool FIRST> DEVI bool partialSM(f32x16& p0, f32x16& p1, float& m_reg, float& alpha) {
;     float pmax = p0[0];
; #pragma unroll
;     for (int r = 1; r < 16; ++r) pmax = fmaxf(pmax, p0[r]);
; #pragma unroll
;     for (int r = 0; r < 16; ++r) pmax = fmaxf(pmax, p1[r]);
;     { auto rr = __builtin_amdgcn_permlane32_swap(__float_as_uint(pmax), __float_as_uint(pmax), false, false);
;       pmax = fmaxf(__uint_as_float(rr[0]), __uint_as_float(rr[1])); }
;     if (FIRST) { m_reg = pmax; alpha = 1.f;
; #pragma unroll
;         for (int r = 0; r < 16; ++r) { p0[r] = __builtin_amdgcn_exp2f(p0[r] - pmax); p1[r] = p1[r] - pmax; }
;         return false;
;     } else if (__builtin_expect(__all(pmax <= ATT_THR), 1)) { alpha = 1.f;
; #pragma unroll
;         for (int r = 0; r < 16; ++r) p0[r] = __builtin_amdgcn_exp2f(p0[r]);
;         return false;
;     } else { const float d = fmaxf(pmax, 0.f); alpha = __builtin_amdgcn_exp2f(-d); m_reg += d;
; #pragma unroll
;         for (int r = 0; r < 16; ++r) { p0[r] = __builtin_amdgcn_exp2f(p0[r] - d); p1[r] = p1[r] - d; }
;         return true;
;     }
; }
; DEVI void finishSM(f32x16& p0, f32x16& p1, float alpha, float& l_reg, bf16x8& pa0, bf16x8& pa1, bf16x8& pa2, bf16x8& pa3) {
; #pragma unroll
;     for (int r = 0; r < 16; ++r) p1[r] = __builtin_amdgcn_exp2f(p1[r]);
;     f32x2 s2 = (f32x2){p0[0], p0[1]} + (f32x2){p1[0], p1[1]};
; #pragma unroll
;     for (int r = 2; r < 16; r += 2) s2 += (f32x2){p0[r], p0[r + 1]} + (f32x2){p1[r], p1[r + 1]};
;     float ps = s2[0] + s2[1];
;     { auto rr = __builtin_amdgcn_permlane32_swap(__float_as_uint(ps), __float_as_uint(ps), false, false);
;       ps = __uint_as_float(rr[0]) + __uint_as_float(rr[1]); }
;     l_reg = l_reg * alpha + ps;
;     ...
;     PK4(p0, 0, pa0); PK4(p0, 8, pa1); PK4(p1, 0, pa2); PK4(p1, 8, pa3);
;     ...
; }
; DEVI void qkt(f32x16& p0, f32x16& p1, const char* Kb, const bf16x8 (&qr)[6], int r32, int hi, const f32x16& cinit) {
; #pragma unroll
;     for (int d0 = 0; d0 < 6; ++d0) { const int cb = (d0 * 16 + hi * 8) * 2;
;         const bf16x8 k0 = *(const bf16x8*)(Kb + KSWZ(r32, cb)), k1 = *(const bf16x8*)(Kb + KSWZ(32 + r32, cb));
;         p0 = __builtin_amdgcn_mfma_f32_32x32x16_bf16(k0, qr[d0], d0 == 0 ? cinit : p0, 0, 0, 0);
;         p1 = __builtin_amdgcn_mfma_f32_32x32x16_bf16(k1, qr[d0], d0 == 0 ? cinit : p1, 0, 0, 0); }
; }
	v_mfma_f32_32x32x16_bf16 v[82:97], v[224:227], v[146:149], v[82:97]
	v_add_f32_e64 v126, v212, v126
	v_add_f32_e64 v127, v213, v127
	v_add_f32_e64 v212, v64, v80
	v_add_f32_e64 v213, v65, v81
	v_cvt_pk_bf16_f32 v64, v78, v79
	v_cvt_pk_bf16_f32 v65, v80, v81
	ds_read_b64_tr_b16 v[66:67], v174 offset:0
	ds_read_b64_tr_b16 v[68:69], v174 offset:0x400
	ds_read_b64_tr_b16 v[70:71], v174 offset:0x800
	ds_read_b64_tr_b16 v[72:73], v174 offset:0xc00
	ds_read_b64_tr_b16 v[74:75], v174 offset:0x1000
	ds_read_b64_tr_b16 v[76:77], v174 offset:0x1400
	ds_read_b64_tr_b16 v[78:79], v174 offset:0x1800
	ds_read_b64_tr_b16 v[80:81], v174 offset:0x1c00
	v_add_f32_e64 v126, v212, v126
	v_add_f32_e64 v127, v213, v127
	ds_read_b64_tr_b16 v[212:213], v174 offset:0x200
	ds_read_b64_tr_b16 v[214:215], v174 offset:0x600
	ds_read_b64_tr_b16 v[216:217], v174 offset:0xa00
	s_waitcnt lgkmcnt(12)
	v_mfma_f32_32x32x16_bf16 v[98:113], v[228:231], v[142:145], v[98:113]
	ds_read_b64_tr_b16 v[218:219], v174 offset:0xe00
	ds_read_b64_tr_b16 v[220:221], v174 offset:0x1200
	ds_read_b64_tr_b16 v[222:223], v174 offset:0x1600
	ds_read_b64_tr_b16 v[224:225], v174 offset:0x1a00
	ds_read_b64_tr_b16 v[226:227], v174 offset:0x1e00
	v_pk_add_f32 v[126:127], v[126:127], v[126:127] op_sel:[0,1] op_sel_hi:[1,0]
	s_waitcnt lgkmcnt(15)
	v_mfma_f32_32x32x16_bf16 v[82:97], v[232:235], v[142:145], v[82:97]
	v_mov_b32_e32 v127, v126
	s_nop 1
	v_permlane32_swap_b32_e32 v126, v127
	s_waitcnt lgkmcnt(14)
	v_mfma_f32_32x32x16_bf16 v[18:33], v[50:53], v[66:69], v[18:33]
	s_waitcnt lgkmcnt(12)
	v_mfma_f32_32x32x16_bf16 v[18:33], v[54:57], v[70:73], v[18:33]
	s_waitcnt lgkmcnt(10)
	v_mfma_f32_32x32x16_bf16 v[18:33], v[58:61], v[74:77], v[18:33]
	s_waitcnt lgkmcnt(8)
	v_mfma_f32_32x32x16_bf16 v[18:33], v[62:65], v[78:81], v[18:33]
	s_waitcnt lgkmcnt(6)
	v_mfma_f32_32x32x16_bf16 v[2:17], v[50:53], v[212:215], v[2:17]
	s_nop 0
	v_max_f32_e32 v249, v99, v99
	v_max_f32_e32 v250, v98, v98
	v_max_f32_e32 v249, v250, v249
	v_max3_f32 v249, v249, v100, v101
	v_max3_f32 v249, v249, v102, v103
	v_max3_f32 v251, v249, v104, v105
	v_max3_f32 v251, v251, v106, v107
	s_waitcnt lgkmcnt(4)
	v_exp_f32_e32 v50, v98
	v_exp_f32_e32 v51, v99
	v_exp_f32_e32 v52, v100
	v_exp_f32_e32 v53, v101
	v_mov_b64_e32 v[66:67], v[82:83]
	v_mov_b64_e32 v[68:69], v[84:85]
	v_mfma_f32_32x32x16_bf16 v[2:17], v[54:57], v[216:219], v[2:17]
	v_max3_f32 v251, v251, v108, v109
	v_max3_f32 v251, v251, v110, v111
	v_max3_f32 v251, v251, v112, v113
	v_max3_f32 v251, v251, v82, v83
	v_max3_f32 v251, v251, v84, v85
	v_max3_f32 v251, v251, v86, v87
	v_max3_f32 v251, v251, v88, v89
	s_waitcnt lgkmcnt(2)
	v_exp_f32_e32 v54, v102
	v_exp_f32_e32 v55, v103
	v_exp_f32_e32 v56, v104
	v_exp_f32_e32 v57, v105
	v_mov_b64_e32 v[70:71], v[86:87]
	v_mov_b64_e32 v[72:73], v[88:89]
	v_mfma_f32_32x32x16_bf16 v[2:17], v[58:61], v[220:223], v[2:17]
	v_max3_f32 v251, v251, v90, v91
	v_max3_f32 v251, v251, v92, v93
	v_max3_f32 v251, v251, v94, v95
	v_max3_f32 v251, v251, v96, v97
	v_mov_b32_e32 v252, v251
	s_nop 1
	v_permlane32_swap_b32_e32 v251, v252
	s_waitcnt lgkmcnt(0)
	v_exp_f32_e32 v58, v106
	v_exp_f32_e32 v59, v107
	v_exp_f32_e32 v60, v108
	v_exp_f32_e32 v61, v109
	v_mov_b64_e32 v[74:75], v[90:91]
	v_mov_b64_e32 v[76:77], v[92:93]
	v_mfma_f32_32x32x16_bf16 v[2:17], v[62:65], v[224:227], v[2:17]
	v_exp_f32_e32 v62, v110
	v_exp_f32_e32 v63, v111
	v_exp_f32_e32 v64, v112
	v_exp_f32_e32 v65, v113
	v_mov_b64_e32 v[78:79], v[94:95]
	v_mov_b64_e32 v[80:81], v[96:97]
	v_max_f32_e32 v252, v252, v252
	v_max_f32_e32 v251, v251, v251
	v_max_f32_e32 v174, v251, v252
	v_cmp_ge_f32_e32 vcc, s80, v174
	s_cmp_lg_u64 vcc, exec
	s_cselect_b64 s[6:7], -1, 0
	s_cbranch_scc1 .LBB0_2275
	v_mov_b32_e32 v203, 1.0
	v_mov_b32_e32 v204, v210
	s_branch .LBB0_2280
